# speedup vs baseline: 1.0323x; 1.0323x over previous
_Z16sum_layer_kernelPKfS0_Pf:
	s_load_dwordx4 s[4:7], s[0:1], 0x0
	s_load_dwordx2 s[8:9], s[0:1], 0x10
	v_lshrrev_b32_e32 v42, 6, v0
	v_bfe_u32 v41, v0, 5, 1
	v_and_b32_e32 v40, 31, v0
	v_readfirstlane_b32 s23, v42
	v_and_b32_e32 v43, 7, v0
	v_bfe_u32 v44, v0, 3, 3
	s_lshl_b32 s3, s2, 12
	s_lshl_b32 s19, s2, 7
	s_lshl_b32 s23, s23, 12
	v_lshlrev_b32_e32 v1, 11, v41
	v_lshl_or_b32 v1, v40, 2, v1
	s_mov_b32 m0, s23
	v_lshrrev_b32_e32 v46, 1, v44
	v_xor_b32_e32 v46, v43, v46
	v_lshlrev_b32_e32 v46, 4, v46
	v_lshl_add_u32 v35, v44, 16, v46
	v_lshl_add_u32 v35, v42, 21, v35
	v_add_u32_e32 v35, s19, v35
	v_xor_b32_e32 v86, 64, v35
	s_mov_b32 s20, 0x7fc00
	s_mov_b32 s21, 0xff800
	s_mov_b32 s22, 0x17f400
	s_mov_b32 s14, 0x200000
	s_mov_b32 s15, 0x20000
	v_and_b32_e32 v45, 63, v0
	v_lshlrev_b32_e32 v37, 4, v45
	s_add_u32 s54, s23, 0x4000
	s_waitcnt lgkmcnt(0)
	s_mov_b32 s12, s6
	s_and_b32 s13, s7, 0xffff
	s_and_b32 s5, s5, 0xffff
	s_mov_b32 s6, 0x800000
	s_mov_b32 s7, s15
	s_mov_b32 m0, s54
	s_nop 0
	buffer_load_dwordx4 v37, s[12:15], s3 offen nt lds
	buffer_load_dwordx4 v37, s[12:15], s3 offen offset:1024 nt lds
	buffer_load_dwordx4 v37, s[12:15], s3 offen offset:2048 nt lds
	buffer_load_dwordx4 v37, s[12:15], s3 offen offset:3072 nt lds
	s_mov_b32 m0, s23
	s_nop 0
	buffer_load_dwordx4 v35, s[4:7], 0 offen nt lds
	buffer_load_dwordx4 v86, s[4:7], s20 offen offset:1024 nt lds
	buffer_load_dwordx4 v35, s[4:7], s21 offen offset:2048 nt lds
	buffer_load_dwordx4 v86, s[4:7], s22 offen offset:3072 nt lds
	v_and_b32_e32 v45, 63, v0
	v_lshlrev_b32_e32 v36, 2, v40
	v_lshl_add_u32 v36, v41, 18, v36
	v_lshl_add_u32 v36, v42, 21, v36
	v_add_u32_e32 v36, s19, v36
	v_bfe_u32 v47, v40, 1, 3
	v_lshlrev_b32_e32 v39, 2, v41
	v_xor_b32_e32 v39, v39, v47
	v_lshlrev_b32_e32 v39, 4, v39
	v_lshl_add_u32 v39, v40, 7, v39
	v_lshl_add_u32 v39, v42, 12, v39
	v_xor_b32_e32 v81, 16, v39
	v_xor_b32_e32 v82, 32, v39
	v_xor_b32_e32 v83, 48, v39
	v_cmp_gt_u32_e32 vcc, 32, v45
	v_mov_b32_e32 v34, 0xc1600000
	v_mov_b32_e32 v84, 0x3fb8aa3b
	v_mov_b32_e32 v85, 0x3f317218
	v_lshlrev_b32_e32 v36, 4, v43
	v_lshl_add_u32 v36, v44, 16, v36
	v_lshl_add_u32 v36, v42, 21, v36
	v_add_u32_e32 v36, s19, v36
	v_mul_u32_u24_e32 v37, 0x1200, v42
	v_add_u32_e32 v37, 0x8000, v37
	v_mul_u32_u24_e32 v38, 0x90, v40
	v_lshlrev_b32_e32 v87, 4, v41
	v_add3_u32 v38, v37, v38, v87
	v_mul_u32_u24_e32 v87, 0x90, v44
	v_lshlrev_b32_e32 v46, 4, v43
	v_add3_u32 v87, v37, v87, v46
	s_mov_b32 s24, 0x80000
	s_mov_b32 s25, 0x100000
	s_mov_b32 s26, 0x180000
	s_and_b32 s9, s9, 0xffff
	s_mov_b32 s10, s6
	s_mov_b32 s11, s15
	v_lshl_add_u32 v0, v42, 12, v1
	v_add_u32_e32 v0, 0x4000, v0
	v_add_u32_e32 v1, 0x400, v0
	s_waitcnt vmcnt(4)
	ds_read2_b32 v[18:19], v0 offset0:0 offset1:32
	ds_read2_b32 v[20:21], v0 offset0:64 offset1:96
	ds_read2_b32 v[22:23], v0 offset0:128 offset1:160
	ds_read2_b32 v[24:25], v0 offset0:192 offset1:224
	ds_read2_b32 v[26:27], v1 offset0:0 offset1:32
	ds_read2_b32 v[28:29], v1 offset0:64 offset1:96
	ds_read2_b32 v[30:31], v1 offset0:128 offset1:160
	ds_read2_b32 v[32:33], v1 offset0:192 offset1:224
	s_waitcnt lgkmcnt(0)
	v_max3_f32 v48, v18, v19, v20
	v_max3_f32 v50, v21, v22, v23
	v_max3_f32 v48, v48, v24, v25
	v_max3_f32 v50, v50, v26, v27
	v_max3_f32 v48, v48, v28, v29
	v_max3_f32 v50, v50, v30, v31
	v_max3_f32 v48, v48, v32, v33
	v_max_f32_e32 v48, v48, v50
	v_mov_b32_e32 v50, v48
	s_nop 1
	v_permlane32_swap_b32_e32 v48, v50
	v_max_f32_e32 v48, v48, v50
	v_fmamk_f32 v48, v48, 0x3fb8aa3b, v34
	v_pk_fma_f32 v[18:19], v[18:19], v[84:85], v[48:49] op_sel_hi:[1,0,0] neg_lo:[0,0,1] neg_hi:[0,0,1]
	v_exp_f32_e32 v18, v18
	v_exp_f32_e32 v19, v19
	v_pk_fma_f32 v[20:21], v[20:21], v[84:85], v[48:49] op_sel_hi:[1,0,0] neg_lo:[0,0,1] neg_hi:[0,0,1]
	v_exp_f32_e32 v20, v20
	v_exp_f32_e32 v21, v21
	v_pk_fma_f32 v[22:23], v[22:23], v[84:85], v[48:49] op_sel_hi:[1,0,0] neg_lo:[0,0,1] neg_hi:[0,0,1]
	v_exp_f32_e32 v22, v22
	v_exp_f32_e32 v23, v23
	v_pk_fma_f32 v[24:25], v[24:25], v[84:85], v[48:49] op_sel_hi:[1,0,0] neg_lo:[0,0,1] neg_hi:[0,0,1]
	v_exp_f32_e32 v24, v24
	v_exp_f32_e32 v25, v25
	v_pk_fma_f32 v[26:27], v[26:27], v[84:85], v[48:49] op_sel_hi:[1,0,0] neg_lo:[0,0,1] neg_hi:[0,0,1]
	v_exp_f32_e32 v26, v26
	v_exp_f32_e32 v27, v27
	v_pk_fma_f32 v[28:29], v[28:29], v[84:85], v[48:49] op_sel_hi:[1,0,0] neg_lo:[0,0,1] neg_hi:[0,0,1]
	v_exp_f32_e32 v28, v28
	v_exp_f32_e32 v29, v29
	v_pk_fma_f32 v[30:31], v[30:31], v[84:85], v[48:49] op_sel_hi:[1,0,0] neg_lo:[0,0,1] neg_hi:[0,0,1]
	v_exp_f32_e32 v30, v30
	v_exp_f32_e32 v31, v31
	v_pk_fma_f32 v[32:33], v[32:33], v[84:85], v[48:49] op_sel_hi:[1,0,0] neg_lo:[0,0,1] neg_hi:[0,0,1]
	v_exp_f32_e32 v32, v32
	v_exp_f32_e32 v33, v33
	v_pk_add_f32 v[56:57], v[18:19], v[20:21]
	v_pk_add_f32 v[58:59], v[22:23], v[24:25]
	v_pk_add_f32 v[60:61], v[26:27], v[28:29]
	v_pk_add_f32 v[62:63], v[30:31], v[32:33]
	v_pk_add_f32 v[56:57], v[56:57], v[58:59]
	v_pk_add_f32 v[60:61], v[60:61], v[62:63]
	v_pk_add_f32 v[56:57], v[56:57], v[60:61]
	v_add_f32_e32 v50, v56, v57
	v_mov_b32_e32 v51, v50
	s_nop 1
	v_permlane32_swap_b32_e32 v50, v51
	v_add_f32_e32 v50, v50, v51
	v_log_f32_e32 v50, v50
	v_cvt_pk_f16_f32 v40, v18, v19
	v_cvt_pk_f16_f32 v41, v20, v21
	v_cvt_pk_f16_f32 v42, v22, v23
	v_cvt_pk_f16_f32 v43, v24, v25
	v_cvt_pk_f16_f32 v44, v26, v27
	v_cvt_pk_f16_f32 v45, v28, v29
	v_cvt_pk_f16_f32 v46, v30, v31
	v_cvt_pk_f16_f32 v47, v32, v33
	v_add_f32_e32 v50, 0x41600000, v50
	v_mul_f32_e32 v50, 0xbf317218, v50
	v_cndmask_b32_e64 v51, v50, 1.0, vcc
	s_waitcnt vmcnt(0)
	ds_read_b128 v[2:5], v39
	ds_read_b128 v[6:9], v81
	ds_read_b128 v[10:13], v82
	ds_read_b128 v[14:17], v83
	s_waitcnt lgkmcnt(2)
	v_max3_f32 v52, v2, v3, v4
	v_max3_f32 v53, v5, v6, v7
	v_max_f32_e32 v52, v52, v8
	v_max_f32_e32 v53, v53, v9
	s_waitcnt lgkmcnt(0)
	v_max3_f32 v52, v52, v10, v11
	v_max3_f32 v53, v53, v12, v13
	v_max3_f32 v52, v52, v14, v15
	v_max3_f32 v53, v53, v16, v17
	v_max_f32_e32 v52, v52, v53
	v_mov_b32_e32 v53, v52
	s_nop 1
	v_permlane32_swap_b32_e32 v52, v53
	v_max_f32_e32 v52, v52, v53
	v_cndmask_b32_e32 v54, 1.0, v52, vcc
	v_fmamk_f32 v48, v52, 0x3fb8aa3b, v34
	v_pk_fma_f32 v[2:3], v[2:3], v[84:85], v[48:49] op_sel_hi:[1,0,0] neg_lo:[0,0,1] neg_hi:[0,0,1]
	v_mfma_f32_32x32x2_f32 v[64:79], v51, v54, 0
	v_exp_f32_e32 v2, v2
	v_exp_f32_e32 v3, v3
	v_pk_fma_f32 v[4:5], v[4:5], v[84:85], v[48:49] op_sel_hi:[1,0,0] neg_lo:[0,0,1] neg_hi:[0,0,1]
	v_exp_f32_e32 v4, v4
	v_exp_f32_e32 v5, v5
	v_pk_fma_f32 v[6:7], v[6:7], v[84:85], v[48:49] op_sel_hi:[1,0,0] neg_lo:[0,0,1] neg_hi:[0,0,1]
	v_exp_f32_e32 v6, v6
	v_exp_f32_e32 v7, v7
	v_pk_fma_f32 v[8:9], v[8:9], v[84:85], v[48:49] op_sel_hi:[1,0,0] neg_lo:[0,0,1] neg_hi:[0,0,1]
	v_exp_f32_e32 v8, v8
	v_exp_f32_e32 v9, v9
	v_pk_fma_f32 v[10:11], v[10:11], v[84:85], v[48:49] op_sel_hi:[1,0,0] neg_lo:[0,0,1] neg_hi:[0,0,1]
	v_exp_f32_e32 v10, v10
	v_cvt_pk_f16_f32 v56, v2, v3
	v_cvt_pk_f16_f32 v57, v4, v5
	v_cvt_pk_f16_f32 v58, v6, v7
	v_cvt_pk_f16_f32 v59, v8, v9
	v_exp_f32_e32 v11, v11
	v_pk_fma_f32 v[12:13], v[12:13], v[84:85], v[48:49] op_sel_hi:[1,0,0] neg_lo:[0,0,1] neg_hi:[0,0,1]
	v_exp_f32_e32 v12, v12
	v_mfma_f32_32x32x16_f16 v[18:33], v[40:43], v[56:59], 0
	v_exp_f32_e32 v13, v13
	v_pk_fma_f32 v[14:15], v[14:15], v[84:85], v[48:49] op_sel_hi:[1,0,0] neg_lo:[0,0,1] neg_hi:[0,0,1]
	v_exp_f32_e32 v14, v14
	v_exp_f32_e32 v15, v15
	v_pk_fma_f32 v[16:17], v[16:17], v[84:85], v[48:49] op_sel_hi:[1,0,0] neg_lo:[0,0,1] neg_hi:[0,0,1]
	v_exp_f32_e32 v16, v16
	v_exp_f32_e32 v17, v17
	v_cvt_pk_f16_f32 v60, v10, v11
	v_cvt_pk_f16_f32 v61, v12, v13
	v_cvt_pk_f16_f32 v62, v14, v15
	v_cvt_pk_f16_f32 v63, v16, v17
	s_nop 1
	v_mfma_f32_32x32x16_f16 v[18:33], v[44:47], v[60:63], v[18:33]
	s_nop 11
	v_log_f32_e32 v18, v18
	v_log_f32_e32 v19, v19
	v_log_f32_e32 v20, v20
	v_log_f32_e32 v21, v21
	v_log_f32_e32 v22, v22
	v_log_f32_e32 v23, v23
	v_log_f32_e32 v24, v24
	v_log_f32_e32 v25, v25
	v_pk_fma_f32 v[64:65], v[18:19], v[84:85], v[64:65] op_sel:[0,1,0] op_sel_hi:[1,1,1]
	v_log_f32_e32 v26, v26
	v_log_f32_e32 v27, v27
	v_pk_fma_f32 v[66:67], v[20:21], v[84:85], v[66:67] op_sel:[0,1,0] op_sel_hi:[1,1,1]
	ds_write_b128 v38, v[64:67]
	v_log_f32_e32 v28, v28
	v_log_f32_e32 v29, v29
	v_pk_fma_f32 v[68:69], v[22:23], v[84:85], v[68:69] op_sel:[0,1,0] op_sel_hi:[1,1,1]
	v_log_f32_e32 v30, v30
	v_log_f32_e32 v31, v31
	v_pk_fma_f32 v[70:71], v[24:25], v[84:85], v[70:71] op_sel:[0,1,0] op_sel_hi:[1,1,1]
	ds_write_b128 v38, v[68:71] offset:32
	v_log_f32_e32 v32, v32
	v_log_f32_e32 v33, v33
	v_pk_fma_f32 v[72:73], v[26:27], v[84:85], v[72:73] op_sel:[0,1,0] op_sel_hi:[1,1,1]
	v_pk_fma_f32 v[74:75], v[28:29], v[84:85], v[74:75] op_sel:[0,1,0] op_sel_hi:[1,1,1]
	ds_write_b128 v38, v[72:75] offset:64
	v_pk_fma_f32 v[76:77], v[30:31], v[84:85], v[76:77] op_sel:[0,1,0] op_sel_hi:[1,1,1]
	v_pk_fma_f32 v[78:79], v[32:33], v[84:85], v[78:79] op_sel:[0,1,0] op_sel_hi:[1,1,1]
	ds_write_b128 v38, v[76:79] offset:96
	ds_read_b128 v[18:21], v87
	ds_read_b128 v[22:25], v87 offset:1152
	ds_read_b128 v[26:29], v87 offset:2304
	ds_read_b128 v[30:33], v87 offset:3456
	s_waitcnt lgkmcnt(3)
	buffer_store_dwordx4 v[18:21], v36, s[8:11], 0 offen sc0 sc1
	s_waitcnt lgkmcnt(2)
	buffer_store_dwordx4 v[22:25], v36, s[8:11], s24 offen sc0 sc1
	s_waitcnt lgkmcnt(1)
	buffer_store_dwordx4 v[26:29], v36, s[8:11], s25 offen sc0 sc1
	s_waitcnt lgkmcnt(0)
	buffer_store_dwordx4 v[30:33], v36, s[8:11], s26 offen sc0 sc1
	s_endpgm
